# residual epilogues of FFN-down and LRU-out: the 16 residual loads of a unit issued up front into dead fragment registers behind counted waits (was one load in flight at a time), on top of unscaled fp8
# speedup vs baseline: 1.0138x; 1.0022x over previous
.LBB0_878:
	v_lshl_add_u32 v18, s77, 8, v171
	v_lshl_or_b32 v2, s78, 8, v191
	v_ashrrev_i32_e32 v19, 31, v18
	v_ashrrev_i32_e32 v3, 31, v2
	v_lshlrev_b64 v[4:5], 11, v[18:19]
	v_lshl_add_u64 v[4:5], s[14:15], 0, v[4:5]
	v_lshlrev_b64 v[20:21], 1, v[2:3]
	v_lshl_add_u64 v[30:31], v[4:5], 0, v[20:21]
	s_lshl_b64 s[40:41], s[40:41], 2
	s_add_u32 s40, s55, s40
	s_addc_u32 s41, s56, s41
	v_lshl_add_u64 v[6:7], v[2:3], 2, s[40:41]
	global_load_dwordx4 v[14:17], v[6:7], off
	global_load_dwordx4 v[10:13], v[6:7], off offset:16
	global_load_dwordx4 v[2:5], v[6:7], off offset:528
	s_nop 0
	global_load_dwordx4 v[6:9], v[6:7], off offset:512
	s_mov_b64 s[100:101], 0x8000
	v_mov_b32_e32 v32, v30
	v_mov_b32_e32 v33, v31
	global_load_dwordx4 v[182:185], v[30:31], off
	global_load_dwordx4 v[186:189], v[30:31], off offset:256
	v_lshl_add_u64 v[30:31], v[30:31], 0, s[100:101]
	global_load_dwordx4 v[196:199], v[30:31], off
	global_load_dwordx4 v[200:203], v[30:31], off offset:256
	v_lshl_add_u64 v[30:31], v[30:31], 0, s[100:101]
	global_load_dwordx4 v[204:207], v[30:31], off
	global_load_dwordx4 v[208:211], v[30:31], off offset:256
	v_lshl_add_u64 v[30:31], v[30:31], 0, s[100:101]
	global_load_dwordx4 v[212:215], v[30:31], off
	global_load_dwordx4 v[216:219], v[30:31], off offset:256
	v_lshl_add_u64 v[30:31], v[30:31], 0, s[100:101]
	v_lshl_add_u64 v[30:31], v[30:31], 0, s[100:101]
	v_lshl_add_u64 v[30:31], v[30:31], 0, s[100:101]
	v_lshl_add_u64 v[30:31], v[30:31], 0, s[100:101]
	v_lshl_add_u64 v[30:31], v[30:31], 0, s[100:101]
	global_load_dwordx4 v[220:223], v[30:31], off
	global_load_dwordx4 v[224:227], v[30:31], off offset:256
	v_lshl_add_u64 v[30:31], v[30:31], 0, s[100:101]
	global_load_dwordx4 v[230:233], v[30:31], off
	global_load_dwordx4 v[234:237], v[30:31], off offset:256
	v_lshl_add_u64 v[30:31], v[30:31], 0, s[100:101]
	global_load_dwordx4 v[238:241], v[30:31], off
	global_load_dwordx4 v[242:245], v[30:31], off offset:256
	v_lshl_add_u64 v[30:31], v[30:31], 0, s[100:101]
	global_load_dwordx4 v[246:249], v[30:31], off
	s_andn2_b64 vcc, exec, s[0:1]
	s_mov_b64 s[0:1], -1
	s_waitcnt vmcnt(15)
	s_mov_b32 s98, 0x3c800000
	v_pk_mul_f32 v[2:3], v[2:3], s[98:99] op_sel_hi:[1,0]
	v_pk_mul_f32 v[4:5], v[4:5], s[98:99] op_sel_hi:[1,0]
	v_pk_mul_f32 v[6:7], v[6:7], s[98:99] op_sel_hi:[1,0]
	v_pk_mul_f32 v[8:9], v[8:9], s[98:99] op_sel_hi:[1,0]
	v_pk_mul_f32 v[10:11], v[10:11], s[98:99] op_sel_hi:[1,0]
	v_pk_mul_f32 v[12:13], v[12:13], s[98:99] op_sel_hi:[1,0]
	v_pk_mul_f32 v[14:15], v[14:15], s[98:99] op_sel_hi:[1,0]
	v_pk_mul_f32 v[16:17], v[16:17], s[98:99] op_sel_hi:[1,0]
	s_waitcnt vmcnt(14)
	v_lshlrev_b32_e32 v18, 16, v182
	v_and_b32_e32 v19, 0xffff0000, v182
	v_lshlrev_b32_e32 v20, 16, v183
	v_and_b32_e32 v21, 0xffff0000, v183
	v_lshlrev_b32_e32 v22, 16, v184
	v_and_b32_e32 v23, 0xffff0000, v184
	v_lshlrev_b32_e32 v24, 16, v185
	v_and_b32_e32 v25, 0xffff0000, v185
	v_pk_fma_f32 v[158:159], v[158:159], v[14:15], v[18:19]
	v_pk_fma_f32 v[160:161], v[160:161], v[16:17], v[20:21]
	v_pk_fma_f32 v[154:155], v[154:155], v[10:11], v[22:23]
	v_pk_fma_f32 v[156:157], v[156:157], v[12:13], v[24:25]
	global_load_dwordx4 v[182:185], v[30:31], off offset:256
	v_cvt_pk_bf16_f32 v158, v158, v159
	v_cvt_pk_bf16_f32 v159, v160, v161
	v_cvt_pk_bf16_f32 v160, v154, v155
	v_cvt_pk_bf16_f32 v161, v156, v157
	global_store_dwordx4 v[32:33], v[158:161], off
	s_waitcnt vmcnt(15)
	v_lshlrev_b32_e32 v18, 16, v186
	v_and_b32_e32 v19, 0xffff0000, v186
	v_lshlrev_b32_e32 v20, 16, v187
	v_and_b32_e32 v21, 0xffff0000, v187
	v_lshlrev_b32_e32 v22, 16, v188
	v_and_b32_e32 v23, 0xffff0000, v188
	v_lshlrev_b32_e32 v24, 16, v189
	v_and_b32_e32 v25, 0xffff0000, v189
	v_pk_fma_f32 v[150:151], v[150:151], v[6:7], v[18:19]
	v_pk_fma_f32 v[152:153], v[152:153], v[8:9], v[20:21]
	v_pk_fma_f32 v[142:143], v[142:143], v[2:3], v[22:23]
	v_pk_fma_f32 v[144:145], v[144:145], v[4:5], v[24:25]
	v_cvt_pk_bf16_f32 v150, v150, v151
	v_cvt_pk_bf16_f32 v151, v152, v153
	v_cvt_pk_bf16_f32 v152, v142, v143
	v_cvt_pk_bf16_f32 v153, v144, v145
	global_store_dwordx4 v[32:33], v[150:153], off offset:256
	s_waitcnt vmcnt(15)
	v_lshlrev_b32_e32 v18, 16, v196
	v_and_b32_e32 v19, 0xffff0000, v196
	v_lshlrev_b32_e32 v20, 16, v197
	v_and_b32_e32 v21, 0xffff0000, v197
	v_lshlrev_b32_e32 v22, 16, v198
	v_and_b32_e32 v23, 0xffff0000, v198
	v_lshlrev_b32_e32 v24, 16, v199
	v_and_b32_e32 v25, 0xffff0000, v199
	v_pk_fma_f32 v[146:147], v[146:147], v[14:15], v[18:19]
	v_pk_fma_f32 v[148:149], v[148:149], v[16:17], v[20:21]
	v_pk_fma_f32 v[138:139], v[138:139], v[10:11], v[22:23]
	v_pk_fma_f32 v[140:141], v[140:141], v[12:13], v[24:25]
	v_cvt_pk_bf16_f32 v146, v146, v147
	v_cvt_pk_bf16_f32 v147, v148, v149
	v_cvt_pk_bf16_f32 v148, v138, v139
	v_cvt_pk_bf16_f32 v149, v140, v141
	v_lshl_add_u64 v[32:33], v[32:33], 0, s[100:101]
	global_store_dwordx4 v[32:33], v[146:149], off
	s_waitcnt vmcnt(15)
	v_lshlrev_b32_e32 v18, 16, v200
	v_and_b32_e32 v19, 0xffff0000, v200
	v_lshlrev_b32_e32 v20, 16, v201
	v_and_b32_e32 v21, 0xffff0000, v201
	v_lshlrev_b32_e32 v22, 16, v202
	v_and_b32_e32 v23, 0xffff0000, v202
	v_lshlrev_b32_e32 v24, 16, v203
	v_and_b32_e32 v25, 0xffff0000, v203
	v_pk_fma_f32 v[134:135], v[134:135], v[6:7], v[18:19]
	v_pk_fma_f32 v[136:137], v[136:137], v[8:9], v[20:21]
	v_pk_fma_f32 v[126:127], v[126:127], v[2:3], v[22:23]
	v_pk_fma_f32 v[128:129], v[128:129], v[4:5], v[24:25]
	v_cvt_pk_bf16_f32 v134, v134, v135
	v_cvt_pk_bf16_f32 v135, v136, v137
	v_cvt_pk_bf16_f32 v136, v126, v127
	v_cvt_pk_bf16_f32 v137, v128, v129
	global_store_dwordx4 v[32:33], v[134:137], off offset:256
	s_waitcnt vmcnt(15)
	v_lshlrev_b32_e32 v18, 16, v204
	v_and_b32_e32 v19, 0xffff0000, v204
	v_lshlrev_b32_e32 v20, 16, v205
	v_and_b32_e32 v21, 0xffff0000, v205
	v_lshlrev_b32_e32 v22, 16, v206
	v_and_b32_e32 v23, 0xffff0000, v206
	v_lshlrev_b32_e32 v24, 16, v207
	v_and_b32_e32 v25, 0xffff0000, v207
	v_pk_fma_f32 v[130:131], v[130:131], v[14:15], v[18:19]
	v_pk_fma_f32 v[132:133], v[132:133], v[16:17], v[20:21]
	v_pk_fma_f32 v[122:123], v[122:123], v[10:11], v[22:23]
	v_pk_fma_f32 v[124:125], v[124:125], v[12:13], v[24:25]
	v_cvt_pk_bf16_f32 v130, v130, v131
	v_cvt_pk_bf16_f32 v131, v132, v133
	v_cvt_pk_bf16_f32 v132, v122, v123
	v_cvt_pk_bf16_f32 v133, v124, v125
	v_lshl_add_u64 v[32:33], v[32:33], 0, s[100:101]
	global_store_dwordx4 v[32:33], v[130:133], off
	s_waitcnt vmcnt(15)
	v_lshlrev_b32_e32 v18, 16, v208
	v_and_b32_e32 v19, 0xffff0000, v208
	v_lshlrev_b32_e32 v20, 16, v209
	v_and_b32_e32 v21, 0xffff0000, v209
	v_lshlrev_b32_e32 v22, 16, v210
	v_and_b32_e32 v23, 0xffff0000, v210
	v_lshlrev_b32_e32 v24, 16, v211
	v_and_b32_e32 v25, 0xffff0000, v211
	v_pk_fma_f32 v[118:119], v[118:119], v[6:7], v[18:19]
	v_pk_fma_f32 v[120:121], v[120:121], v[8:9], v[20:21]
	v_pk_fma_f32 v[110:111], v[110:111], v[2:3], v[22:23]
	v_pk_fma_f32 v[112:113], v[112:113], v[4:5], v[24:25]
	v_cvt_pk_bf16_f32 v118, v118, v119
	v_cvt_pk_bf16_f32 v119, v120, v121
	v_cvt_pk_bf16_f32 v120, v110, v111
	v_cvt_pk_bf16_f32 v121, v112, v113
	global_store_dwordx4 v[32:33], v[118:121], off offset:256
	s_waitcnt vmcnt(15)
	v_lshlrev_b32_e32 v18, 16, v212
	v_and_b32_e32 v19, 0xffff0000, v212
	v_lshlrev_b32_e32 v20, 16, v213
	v_and_b32_e32 v21, 0xffff0000, v213
	v_lshlrev_b32_e32 v22, 16, v214
	v_and_b32_e32 v23, 0xffff0000, v214
	v_lshlrev_b32_e32 v24, 16, v215
	v_and_b32_e32 v25, 0xffff0000, v215
	v_pk_fma_f32 v[114:115], v[114:115], v[14:15], v[18:19]
	v_pk_fma_f32 v[116:117], v[116:117], v[16:17], v[20:21]
	v_pk_fma_f32 v[106:107], v[106:107], v[10:11], v[22:23]
	v_pk_fma_f32 v[108:109], v[108:109], v[12:13], v[24:25]
	v_cvt_pk_bf16_f32 v114, v114, v115
	v_cvt_pk_bf16_f32 v115, v116, v117
	v_cvt_pk_bf16_f32 v116, v106, v107
	v_cvt_pk_bf16_f32 v117, v108, v109
	v_lshl_add_u64 v[32:33], v[32:33], 0, s[100:101]
	global_store_dwordx4 v[32:33], v[114:117], off
	s_waitcnt vmcnt(15)
	v_lshlrev_b32_e32 v18, 16, v216
	v_and_b32_e32 v19, 0xffff0000, v216
	v_lshlrev_b32_e32 v20, 16, v217
	v_and_b32_e32 v21, 0xffff0000, v217
	v_lshlrev_b32_e32 v22, 16, v218
	v_and_b32_e32 v23, 0xffff0000, v218
	v_lshlrev_b32_e32 v24, 16, v219
	v_and_b32_e32 v25, 0xffff0000, v219
	v_pk_fma_f32 v[102:103], v[102:103], v[6:7], v[18:19]
	v_pk_fma_f32 v[104:105], v[104:105], v[8:9], v[20:21]
	v_pk_fma_f32 v[98:99], v[98:99], v[2:3], v[22:23]
	v_pk_fma_f32 v[100:101], v[100:101], v[4:5], v[24:25]
	v_cvt_pk_bf16_f32 v102, v102, v103
	v_cvt_pk_bf16_f32 v103, v104, v105
	v_cvt_pk_bf16_f32 v104, v98, v99
	v_cvt_pk_bf16_f32 v105, v100, v101
	global_store_dwordx4 v[32:33], v[102:105], off offset:256
	s_waitcnt vmcnt(15)
	v_lshlrev_b32_e32 v18, 16, v220
	v_and_b32_e32 v19, 0xffff0000, v220
	v_lshlrev_b32_e32 v20, 16, v221
	v_and_b32_e32 v21, 0xffff0000, v221
	v_lshlrev_b32_e32 v22, 16, v222
	v_and_b32_e32 v23, 0xffff0000, v222
	v_lshlrev_b32_e32 v24, 16, v223
	v_and_b32_e32 v25, 0xffff0000, v223
	v_pk_fma_f32 v[94:95], v[94:95], v[14:15], v[18:19]
	v_pk_fma_f32 v[96:97], v[96:97], v[16:17], v[20:21]
	v_pk_fma_f32 v[90:91], v[90:91], v[10:11], v[22:23]
	v_pk_fma_f32 v[92:93], v[92:93], v[12:13], v[24:25]
	v_cvt_pk_bf16_f32 v94, v94, v95
	v_cvt_pk_bf16_f32 v95, v96, v97
	v_cvt_pk_bf16_f32 v96, v90, v91
	v_cvt_pk_bf16_f32 v97, v92, v93
	v_lshl_add_u64 v[32:33], v[32:33], 0, s[100:101]
	v_lshl_add_u64 v[32:33], v[32:33], 0, s[100:101]
	v_lshl_add_u64 v[32:33], v[32:33], 0, s[100:101]
	v_lshl_add_u64 v[32:33], v[32:33], 0, s[100:101]
	v_lshl_add_u64 v[32:33], v[32:33], 0, s[100:101]
	global_store_dwordx4 v[32:33], v[94:97], off
	s_waitcnt vmcnt(15)
	v_lshlrev_b32_e32 v18, 16, v224
	v_and_b32_e32 v19, 0xffff0000, v224
	v_lshlrev_b32_e32 v20, 16, v225
	v_and_b32_e32 v21, 0xffff0000, v225
	v_lshlrev_b32_e32 v22, 16, v226
	v_and_b32_e32 v23, 0xffff0000, v226
	v_lshlrev_b32_e32 v24, 16, v227
	v_and_b32_e32 v25, 0xffff0000, v227
	v_pk_fma_f32 v[86:87], v[86:87], v[6:7], v[18:19]
	v_pk_fma_f32 v[88:89], v[88:89], v[8:9], v[20:21]
	v_pk_fma_f32 v[78:79], v[78:79], v[2:3], v[22:23]
	v_pk_fma_f32 v[80:81], v[80:81], v[4:5], v[24:25]
	v_cvt_pk_bf16_f32 v86, v86, v87
	v_cvt_pk_bf16_f32 v87, v88, v89
	v_cvt_pk_bf16_f32 v88, v78, v79
	v_cvt_pk_bf16_f32 v89, v80, v81
	global_store_dwordx4 v[32:33], v[86:89], off offset:256
	s_waitcnt vmcnt(15)
	v_lshlrev_b32_e32 v18, 16, v230
	v_and_b32_e32 v19, 0xffff0000, v230
	v_lshlrev_b32_e32 v20, 16, v231
	v_and_b32_e32 v21, 0xffff0000, v231
	v_lshlrev_b32_e32 v22, 16, v232
	v_and_b32_e32 v23, 0xffff0000, v232
	v_lshlrev_b32_e32 v24, 16, v233
	v_and_b32_e32 v25, 0xffff0000, v233
	v_pk_fma_f32 v[82:83], v[82:83], v[14:15], v[18:19]
	v_pk_fma_f32 v[84:85], v[84:85], v[16:17], v[20:21]
	v_pk_fma_f32 v[74:75], v[74:75], v[10:11], v[22:23]
	v_pk_fma_f32 v[76:77], v[76:77], v[12:13], v[24:25]
	v_cvt_pk_bf16_f32 v82, v82, v83
	v_cvt_pk_bf16_f32 v83, v84, v85
	v_cvt_pk_bf16_f32 v84, v74, v75
	v_cvt_pk_bf16_f32 v85, v76, v77
	v_lshl_add_u64 v[32:33], v[32:33], 0, s[100:101]
	global_store_dwordx4 v[32:33], v[82:85], off
	s_waitcnt vmcnt(15)
	v_lshlrev_b32_e32 v18, 16, v234
	v_and_b32_e32 v19, 0xffff0000, v234
	v_lshlrev_b32_e32 v20, 16, v235
	v_and_b32_e32 v21, 0xffff0000, v235
	v_lshlrev_b32_e32 v22, 16, v236
	v_and_b32_e32 v23, 0xffff0000, v236
	v_lshlrev_b32_e32 v24, 16, v237
	v_and_b32_e32 v25, 0xffff0000, v237
	v_pk_fma_f32 v[70:71], v[70:71], v[6:7], v[18:19]
	v_pk_fma_f32 v[72:73], v[72:73], v[8:9], v[20:21]
	v_pk_fma_f32 v[62:63], v[62:63], v[2:3], v[22:23]
	v_pk_fma_f32 v[64:65], v[64:65], v[4:5], v[24:25]
	v_cvt_pk_bf16_f32 v70, v70, v71
	v_cvt_pk_bf16_f32 v71, v72, v73
	v_cvt_pk_bf16_f32 v72, v62, v63
	v_cvt_pk_bf16_f32 v73, v64, v65
	global_store_dwordx4 v[32:33], v[70:73], off offset:256
	s_waitcnt vmcnt(15)
	v_lshlrev_b32_e32 v18, 16, v238
	v_and_b32_e32 v19, 0xffff0000, v238
	v_lshlrev_b32_e32 v20, 16, v239
	v_and_b32_e32 v21, 0xffff0000, v239
	v_lshlrev_b32_e32 v22, 16, v240
	v_and_b32_e32 v23, 0xffff0000, v240
	v_lshlrev_b32_e32 v24, 16, v241
	v_and_b32_e32 v25, 0xffff0000, v241
	v_pk_fma_f32 v[66:67], v[66:67], v[14:15], v[18:19]
	v_pk_fma_f32 v[68:69], v[68:69], v[16:17], v[20:21]
	v_pk_fma_f32 v[58:59], v[58:59], v[10:11], v[22:23]
	v_pk_fma_f32 v[60:61], v[60:61], v[12:13], v[24:25]
	v_cvt_pk_bf16_f32 v66, v66, v67
	v_cvt_pk_bf16_f32 v67, v68, v69
	v_cvt_pk_bf16_f32 v68, v58, v59
	v_cvt_pk_bf16_f32 v69, v60, v61
	v_lshl_add_u64 v[32:33], v[32:33], 0, s[100:101]
	global_store_dwordx4 v[32:33], v[66:69], off
	s_waitcnt vmcnt(15)
	v_lshlrev_b32_e32 v18, 16, v242
	v_and_b32_e32 v19, 0xffff0000, v242
	v_lshlrev_b32_e32 v20, 16, v243
	v_and_b32_e32 v21, 0xffff0000, v243
	v_lshlrev_b32_e32 v22, 16, v244
	v_and_b32_e32 v23, 0xffff0000, v244
	v_lshlrev_b32_e32 v24, 16, v245
	v_and_b32_e32 v25, 0xffff0000, v245
	v_pk_fma_f32 v[54:55], v[54:55], v[6:7], v[18:19]
	v_pk_fma_f32 v[56:57], v[56:57], v[8:9], v[20:21]
	v_pk_fma_f32 v[46:47], v[46:47], v[2:3], v[22:23]
	v_pk_fma_f32 v[48:49], v[48:49], v[4:5], v[24:25]
	v_cvt_pk_bf16_f32 v54, v54, v55
	v_cvt_pk_bf16_f32 v55, v56, v57
	v_cvt_pk_bf16_f32 v56, v46, v47
	v_cvt_pk_bf16_f32 v57, v48, v49
	global_store_dwordx4 v[32:33], v[54:57], off offset:256
	s_waitcnt vmcnt(15)
	v_lshlrev_b32_e32 v18, 16, v246
	v_and_b32_e32 v19, 0xffff0000, v246
	v_lshlrev_b32_e32 v20, 16, v247
	v_and_b32_e32 v21, 0xffff0000, v247
	v_lshlrev_b32_e32 v22, 16, v248
	v_and_b32_e32 v23, 0xffff0000, v248
	v_lshlrev_b32_e32 v24, 16, v249
	v_and_b32_e32 v25, 0xffff0000, v249
	v_pk_fma_f32 v[50:51], v[50:51], v[14:15], v[18:19]
	v_pk_fma_f32 v[52:53], v[52:53], v[16:17], v[20:21]
	v_pk_fma_f32 v[42:43], v[42:43], v[10:11], v[22:23]
	v_pk_fma_f32 v[44:45], v[44:45], v[12:13], v[24:25]
	v_cvt_pk_bf16_f32 v50, v50, v51
	v_cvt_pk_bf16_f32 v51, v52, v53
	v_cvt_pk_bf16_f32 v52, v42, v43
	v_cvt_pk_bf16_f32 v53, v44, v45
	v_lshl_add_u64 v[32:33], v[32:33], 0, s[100:101]
	global_store_dwordx4 v[32:33], v[50:53], off
	s_waitcnt vmcnt(15)
	v_lshlrev_b32_e32 v18, 16, v182
	v_and_b32_e32 v19, 0xffff0000, v182
	v_lshlrev_b32_e32 v20, 16, v183
	v_and_b32_e32 v21, 0xffff0000, v183
	v_lshlrev_b32_e32 v22, 16, v184
	v_and_b32_e32 v23, 0xffff0000, v184
	v_lshlrev_b32_e32 v24, 16, v185
	v_and_b32_e32 v25, 0xffff0000, v185
	v_pk_fma_f32 v[38:39], v[38:39], v[6:7], v[18:19]
	v_pk_fma_f32 v[40:41], v[40:41], v[8:9], v[20:21]
	v_pk_fma_f32 v[34:35], v[34:35], v[2:3], v[22:23]
	v_pk_fma_f32 v[36:37], v[36:37], v[4:5], v[24:25]
	v_cvt_pk_bf16_f32 v38, v38, v39
	v_cvt_pk_bf16_f32 v39, v40, v41
	v_cvt_pk_bf16_f32 v40, v34, v35
	v_cvt_pk_bf16_f32 v41, v36, v37
	global_store_dwordx4 v[32:33], v[38:41], off offset:256
	s_cbranch_vccnz .LBB0_869
	s_andn2_b64 vcc, exec, s[10:11]
	s_cbranch_vccnz .LBB0_868
	s_barrier
	s_branch .LBB0_868

.LBB0_1636:
	v_lshl_add_u32 v162, s53, 8, v1
	v_lshl_or_b32 v118, s54, 8, v167
	v_ashrrev_i32_e32 v163, 31, v162
	v_ashrrev_i32_e32 v119, 31, v118
	v_lshlrev_b64 v[120:121], 11, v[162:163]
	v_lshl_add_u64 v[120:121], s[14:15], 0, v[120:121]
	v_lshlrev_b64 v[164:165], 1, v[118:119]
	v_lshl_add_u64 v[176:177], v[120:121], 0, v[164:165]
	s_lshl_b64 s[18:19], s[18:19], 2
	s_add_u32 s18, s42, s18
	s_addc_u32 s19, s43, s19
	v_lshl_add_u64 v[126:127], v[118:119], 2, s[18:19]
	global_load_dwordx4 v[134:137], v[126:127], off
	global_load_dwordx4 v[130:133], v[126:127], off offset:16
	global_load_dwordx4 v[118:121], v[126:127], off offset:528
	s_nop 0
	global_load_dwordx4 v[126:129], v[126:127], off offset:512
	s_mov_b64 s[100:101], 0x8000
	v_mov_b32_e32 v164, v176
	v_mov_b32_e32 v165, v177
	global_load_dwordx4 v[182:185], v[176:177], off
	global_load_dwordx4 v[186:189], v[176:177], off offset:256
	v_lshl_add_u64 v[176:177], v[176:177], 0, s[100:101]
	global_load_dwordx4 v[190:193], v[176:177], off
	global_load_dwordx4 v[194:197], v[176:177], off offset:256
	v_lshl_add_u64 v[176:177], v[176:177], 0, s[100:101]
	global_load_dwordx4 v[198:201], v[176:177], off
	global_load_dwordx4 v[202:205], v[176:177], off offset:256
	v_lshl_add_u64 v[176:177], v[176:177], 0, s[100:101]
	global_load_dwordx4 v[206:209], v[176:177], off
	global_load_dwordx4 v[210:213], v[176:177], off offset:256
	v_lshl_add_u64 v[176:177], v[176:177], 0, s[100:101]
	v_lshl_add_u64 v[176:177], v[176:177], 0, s[100:101]
	v_lshl_add_u64 v[176:177], v[176:177], 0, s[100:101]
	v_lshl_add_u64 v[176:177], v[176:177], 0, s[100:101]
	v_lshl_add_u64 v[176:177], v[176:177], 0, s[100:101]
	global_load_dwordx4 v[226:229], v[176:177], off
	global_load_dwordx4 v[230:233], v[176:177], off offset:256
	v_lshl_add_u64 v[176:177], v[176:177], 0, s[100:101]
	global_load_dwordx4 v[234:237], v[176:177], off
	global_load_dwordx4 v[238:241], v[176:177], off offset:256
	v_lshl_add_u64 v[176:177], v[176:177], 0, s[100:101]
	global_load_dwordx4 v[242:245], v[176:177], off
	global_load_dwordx4 v[246:249], v[176:177], off offset:256
	s_andn2_b64 vcc, exec, s[0:1]
	s_mov_b64 s[0:1], -1
	s_waitcnt vmcnt(14)
	s_waitcnt vmcnt(13)
	v_lshlrev_b32_e32 v172, 16, v182
	v_and_b32_e32 v173, 0xffff0000, v182
	v_lshlrev_b32_e32 v174, 16, v183
	v_and_b32_e32 v175, 0xffff0000, v183
	v_lshlrev_b32_e32 v178, 16, v184
	v_and_b32_e32 v179, 0xffff0000, v184
	v_lshlrev_b32_e32 v180, 16, v185
	v_and_b32_e32 v181, 0xffff0000, v185
	v_pk_fma_f32 v[142:143], v[142:143], v[134:135], v[172:173]
	v_pk_fma_f32 v[144:145], v[144:145], v[136:137], v[174:175]
	v_pk_fma_f32 v[138:139], v[138:139], v[130:131], v[178:179]
	v_pk_fma_f32 v[140:141], v[140:141], v[132:133], v[180:181]
	v_lshl_add_u64 v[176:177], v[176:177], 0, s[100:101]
	global_load_dwordx4 v[182:185], v[176:177], off
	v_cvt_pk_bf16_f32 v142, v142, v143
	v_cvt_pk_bf16_f32 v143, v144, v145
	v_cvt_pk_bf16_f32 v144, v138, v139
	v_cvt_pk_bf16_f32 v145, v140, v141
	global_store_dwordx4 v[164:165], v[142:145], off
	s_waitcnt vmcnt(14)
	v_lshlrev_b32_e32 v172, 16, v186
	v_and_b32_e32 v173, 0xffff0000, v186
	v_lshlrev_b32_e32 v174, 16, v187
	v_and_b32_e32 v175, 0xffff0000, v187
	v_lshlrev_b32_e32 v178, 16, v188
	v_and_b32_e32 v179, 0xffff0000, v188
	v_lshlrev_b32_e32 v180, 16, v189
	v_and_b32_e32 v181, 0xffff0000, v189
	v_pk_fma_f32 v[122:123], v[122:123], v[126:127], v[172:173]
	v_pk_fma_f32 v[124:125], v[124:125], v[128:129], v[174:175]
	v_pk_fma_f32 v[110:111], v[110:111], v[118:119], v[178:179]
	v_pk_fma_f32 v[112:113], v[112:113], v[120:121], v[180:181]
	global_load_dwordx4 v[186:189], v[176:177], off offset:256
	v_cvt_pk_bf16_f32 v122, v122, v123
	v_cvt_pk_bf16_f32 v123, v124, v125
	v_cvt_pk_bf16_f32 v124, v110, v111
	v_cvt_pk_bf16_f32 v125, v112, v113
	global_store_dwordx4 v[164:165], v[122:125], off offset:256
	s_waitcnt vmcnt(15)
	v_lshlrev_b32_e32 v172, 16, v190
	v_and_b32_e32 v173, 0xffff0000, v190
	v_lshlrev_b32_e32 v174, 16, v191
	v_and_b32_e32 v175, 0xffff0000, v191
	v_lshlrev_b32_e32 v178, 16, v192
	v_and_b32_e32 v179, 0xffff0000, v192
	v_lshlrev_b32_e32 v180, 16, v193
	v_and_b32_e32 v181, 0xffff0000, v193
	v_pk_fma_f32 v[114:115], v[114:115], v[134:135], v[172:173]
	v_pk_fma_f32 v[116:117], v[116:117], v[136:137], v[174:175]
	v_pk_fma_f32 v[106:107], v[106:107], v[130:131], v[178:179]
	v_pk_fma_f32 v[108:109], v[108:109], v[132:133], v[180:181]
	v_cvt_pk_bf16_f32 v114, v114, v115
	v_cvt_pk_bf16_f32 v115, v116, v117
	v_cvt_pk_bf16_f32 v116, v106, v107
	v_cvt_pk_bf16_f32 v117, v108, v109
	v_lshl_add_u64 v[164:165], v[164:165], 0, s[100:101]
	global_store_dwordx4 v[164:165], v[114:117], off
	s_waitcnt vmcnt(15)
	v_lshlrev_b32_e32 v172, 16, v194
	v_and_b32_e32 v173, 0xffff0000, v194
	v_lshlrev_b32_e32 v174, 16, v195
	v_and_b32_e32 v175, 0xffff0000, v195
	v_lshlrev_b32_e32 v178, 16, v196
	v_and_b32_e32 v179, 0xffff0000, v196
	v_lshlrev_b32_e32 v180, 16, v197
	v_and_b32_e32 v181, 0xffff0000, v197
	v_pk_fma_f32 v[102:103], v[102:103], v[126:127], v[172:173]
	v_pk_fma_f32 v[104:105], v[104:105], v[128:129], v[174:175]
	v_pk_fma_f32 v[94:95], v[94:95], v[118:119], v[178:179]
	v_pk_fma_f32 v[96:97], v[96:97], v[120:121], v[180:181]
	v_cvt_pk_bf16_f32 v102, v102, v103
	v_cvt_pk_bf16_f32 v103, v104, v105
	v_cvt_pk_bf16_f32 v104, v94, v95
	v_cvt_pk_bf16_f32 v105, v96, v97
	global_store_dwordx4 v[164:165], v[102:105], off offset:256
	s_waitcnt vmcnt(15)
	v_lshlrev_b32_e32 v172, 16, v198
	v_and_b32_e32 v173, 0xffff0000, v198
	v_lshlrev_b32_e32 v174, 16, v199
	v_and_b32_e32 v175, 0xffff0000, v199
	v_lshlrev_b32_e32 v178, 16, v200
	v_and_b32_e32 v179, 0xffff0000, v200
	v_lshlrev_b32_e32 v180, 16, v201
	v_and_b32_e32 v181, 0xffff0000, v201
	v_pk_fma_f32 v[98:99], v[98:99], v[134:135], v[172:173]
	v_pk_fma_f32 v[100:101], v[100:101], v[136:137], v[174:175]
	v_pk_fma_f32 v[90:91], v[90:91], v[130:131], v[178:179]
	v_pk_fma_f32 v[92:93], v[92:93], v[132:133], v[180:181]
	v_cvt_pk_bf16_f32 v98, v98, v99
	v_cvt_pk_bf16_f32 v99, v100, v101
	v_cvt_pk_bf16_f32 v100, v90, v91
	v_cvt_pk_bf16_f32 v101, v92, v93
	v_lshl_add_u64 v[164:165], v[164:165], 0, s[100:101]
	global_store_dwordx4 v[164:165], v[98:101], off
	s_waitcnt vmcnt(15)
	v_lshlrev_b32_e32 v172, 16, v202
	v_and_b32_e32 v173, 0xffff0000, v202
	v_lshlrev_b32_e32 v174, 16, v203
	v_and_b32_e32 v175, 0xffff0000, v203
	v_lshlrev_b32_e32 v178, 16, v204
	v_and_b32_e32 v179, 0xffff0000, v204
	v_lshlrev_b32_e32 v180, 16, v205
	v_and_b32_e32 v181, 0xffff0000, v205
	v_pk_fma_f32 v[86:87], v[86:87], v[126:127], v[172:173]
	v_pk_fma_f32 v[88:89], v[88:89], v[128:129], v[174:175]
	v_pk_fma_f32 v[78:79], v[78:79], v[118:119], v[178:179]
	v_pk_fma_f32 v[80:81], v[80:81], v[120:121], v[180:181]
	v_cvt_pk_bf16_f32 v86, v86, v87
	v_cvt_pk_bf16_f32 v87, v88, v89
	v_cvt_pk_bf16_f32 v88, v78, v79
	v_cvt_pk_bf16_f32 v89, v80, v81
	global_store_dwordx4 v[164:165], v[86:89], off offset:256
	s_waitcnt vmcnt(15)
	v_lshlrev_b32_e32 v172, 16, v206
	v_and_b32_e32 v173, 0xffff0000, v206
	v_lshlrev_b32_e32 v174, 16, v207
	v_and_b32_e32 v175, 0xffff0000, v207
	v_lshlrev_b32_e32 v178, 16, v208
	v_and_b32_e32 v179, 0xffff0000, v208
	v_lshlrev_b32_e32 v180, 16, v209
	v_and_b32_e32 v181, 0xffff0000, v209
	v_pk_fma_f32 v[82:83], v[82:83], v[134:135], v[172:173]
	v_pk_fma_f32 v[84:85], v[84:85], v[136:137], v[174:175]
	v_pk_fma_f32 v[74:75], v[74:75], v[130:131], v[178:179]
	v_pk_fma_f32 v[76:77], v[76:77], v[132:133], v[180:181]
	v_cvt_pk_bf16_f32 v82, v82, v83
	v_cvt_pk_bf16_f32 v83, v84, v85
	v_cvt_pk_bf16_f32 v84, v74, v75
	v_cvt_pk_bf16_f32 v85, v76, v77
	v_lshl_add_u64 v[164:165], v[164:165], 0, s[100:101]
	global_store_dwordx4 v[164:165], v[82:85], off
	s_waitcnt vmcnt(15)
	v_lshlrev_b32_e32 v172, 16, v210
	v_and_b32_e32 v173, 0xffff0000, v210
	v_lshlrev_b32_e32 v174, 16, v211
	v_and_b32_e32 v175, 0xffff0000, v211
	v_lshlrev_b32_e32 v178, 16, v212
	v_and_b32_e32 v179, 0xffff0000, v212
	v_lshlrev_b32_e32 v180, 16, v213
	v_and_b32_e32 v181, 0xffff0000, v213
	v_pk_fma_f32 v[70:71], v[70:71], v[126:127], v[172:173]
	v_pk_fma_f32 v[72:73], v[72:73], v[128:129], v[174:175]
	v_pk_fma_f32 v[66:67], v[66:67], v[118:119], v[178:179]
	v_pk_fma_f32 v[68:69], v[68:69], v[120:121], v[180:181]
	v_cvt_pk_bf16_f32 v70, v70, v71
	v_cvt_pk_bf16_f32 v71, v72, v73
	v_cvt_pk_bf16_f32 v72, v66, v67
	v_cvt_pk_bf16_f32 v73, v68, v69
	global_store_dwordx4 v[164:165], v[70:73], off offset:256
	s_waitcnt vmcnt(15)
	v_lshlrev_b32_e32 v172, 16, v226
	v_and_b32_e32 v173, 0xffff0000, v226
	v_lshlrev_b32_e32 v174, 16, v227
	v_and_b32_e32 v175, 0xffff0000, v227
	v_lshlrev_b32_e32 v178, 16, v228
	v_and_b32_e32 v179, 0xffff0000, v228
	v_lshlrev_b32_e32 v180, 16, v229
	v_and_b32_e32 v181, 0xffff0000, v229
	v_pk_fma_f32 v[62:63], v[62:63], v[134:135], v[172:173]
	v_pk_fma_f32 v[64:65], v[64:65], v[136:137], v[174:175]
	v_pk_fma_f32 v[58:59], v[58:59], v[130:131], v[178:179]
	v_pk_fma_f32 v[60:61], v[60:61], v[132:133], v[180:181]
	v_cvt_pk_bf16_f32 v62, v62, v63
	v_cvt_pk_bf16_f32 v63, v64, v65
	v_cvt_pk_bf16_f32 v64, v58, v59
	v_cvt_pk_bf16_f32 v65, v60, v61
	v_lshl_add_u64 v[164:165], v[164:165], 0, s[100:101]
	v_lshl_add_u64 v[164:165], v[164:165], 0, s[100:101]
	v_lshl_add_u64 v[164:165], v[164:165], 0, s[100:101]
	v_lshl_add_u64 v[164:165], v[164:165], 0, s[100:101]
	v_lshl_add_u64 v[164:165], v[164:165], 0, s[100:101]
	global_store_dwordx4 v[164:165], v[62:65], off
	s_waitcnt vmcnt(15)
	v_lshlrev_b32_e32 v172, 16, v230
	v_and_b32_e32 v173, 0xffff0000, v230
	v_lshlrev_b32_e32 v174, 16, v231
	v_and_b32_e32 v175, 0xffff0000, v231
	v_lshlrev_b32_e32 v178, 16, v232
	v_and_b32_e32 v179, 0xffff0000, v232
	v_lshlrev_b32_e32 v180, 16, v233
	v_and_b32_e32 v181, 0xffff0000, v233
	v_pk_fma_f32 v[54:55], v[54:55], v[126:127], v[172:173]
	v_pk_fma_f32 v[56:57], v[56:57], v[128:129], v[174:175]
	v_pk_fma_f32 v[46:47], v[46:47], v[118:119], v[178:179]
	v_pk_fma_f32 v[48:49], v[48:49], v[120:121], v[180:181]
	v_cvt_pk_bf16_f32 v54, v54, v55
	v_cvt_pk_bf16_f32 v55, v56, v57
	v_cvt_pk_bf16_f32 v56, v46, v47
	v_cvt_pk_bf16_f32 v57, v48, v49
	global_store_dwordx4 v[164:165], v[54:57], off offset:256
	s_waitcnt vmcnt(15)
	v_lshlrev_b32_e32 v172, 16, v234
	v_and_b32_e32 v173, 0xffff0000, v234
	v_lshlrev_b32_e32 v174, 16, v235
	v_and_b32_e32 v175, 0xffff0000, v235
	v_lshlrev_b32_e32 v178, 16, v236
	v_and_b32_e32 v179, 0xffff0000, v236
	v_lshlrev_b32_e32 v180, 16, v237
	v_and_b32_e32 v181, 0xffff0000, v237
	v_pk_fma_f32 v[50:51], v[50:51], v[134:135], v[172:173]
	v_pk_fma_f32 v[52:53], v[52:53], v[136:137], v[174:175]
	v_pk_fma_f32 v[42:43], v[42:43], v[130:131], v[178:179]
	v_pk_fma_f32 v[44:45], v[44:45], v[132:133], v[180:181]
	v_cvt_pk_bf16_f32 v50, v50, v51
	v_cvt_pk_bf16_f32 v51, v52, v53
	v_cvt_pk_bf16_f32 v52, v42, v43
	v_cvt_pk_bf16_f32 v53, v44, v45
	v_lshl_add_u64 v[164:165], v[164:165], 0, s[100:101]
	global_store_dwordx4 v[164:165], v[50:53], off
	s_waitcnt vmcnt(15)
	v_lshlrev_b32_e32 v172, 16, v238
	v_and_b32_e32 v173, 0xffff0000, v238
	v_lshlrev_b32_e32 v174, 16, v239
	v_and_b32_e32 v175, 0xffff0000, v239
	v_lshlrev_b32_e32 v178, 16, v240
	v_and_b32_e32 v179, 0xffff0000, v240
	v_lshlrev_b32_e32 v180, 16, v241
	v_and_b32_e32 v181, 0xffff0000, v241
	v_pk_fma_f32 v[38:39], v[38:39], v[126:127], v[172:173]
	v_pk_fma_f32 v[40:41], v[40:41], v[128:129], v[174:175]
	v_pk_fma_f32 v[30:31], v[30:31], v[118:119], v[178:179]
	v_pk_fma_f32 v[32:33], v[32:33], v[120:121], v[180:181]
	v_cvt_pk_bf16_f32 v38, v38, v39
	v_cvt_pk_bf16_f32 v39, v40, v41
	v_cvt_pk_bf16_f32 v40, v30, v31
	v_cvt_pk_bf16_f32 v41, v32, v33
	global_store_dwordx4 v[164:165], v[38:41], off offset:256
	s_waitcnt vmcnt(15)
	v_lshlrev_b32_e32 v172, 16, v242
	v_and_b32_e32 v173, 0xffff0000, v242
	v_lshlrev_b32_e32 v174, 16, v243
	v_and_b32_e32 v175, 0xffff0000, v243
	v_lshlrev_b32_e32 v178, 16, v244
	v_and_b32_e32 v179, 0xffff0000, v244
	v_lshlrev_b32_e32 v180, 16, v245
	v_and_b32_e32 v181, 0xffff0000, v245
	v_pk_fma_f32 v[34:35], v[34:35], v[134:135], v[172:173]
	v_pk_fma_f32 v[36:37], v[36:37], v[136:137], v[174:175]
	v_pk_fma_f32 v[26:27], v[26:27], v[130:131], v[178:179]
	v_pk_fma_f32 v[28:29], v[28:29], v[132:133], v[180:181]
	v_cvt_pk_bf16_f32 v34, v34, v35
	v_cvt_pk_bf16_f32 v35, v36, v37
	v_cvt_pk_bf16_f32 v36, v26, v27
	v_cvt_pk_bf16_f32 v37, v28, v29
	v_lshl_add_u64 v[164:165], v[164:165], 0, s[100:101]
	global_store_dwordx4 v[164:165], v[34:37], off
	s_waitcnt vmcnt(15)
	v_lshlrev_b32_e32 v172, 16, v246
	v_and_b32_e32 v173, 0xffff0000, v246
	v_lshlrev_b32_e32 v174, 16, v247
	v_and_b32_e32 v175, 0xffff0000, v247
	v_lshlrev_b32_e32 v178, 16, v248
	v_and_b32_e32 v179, 0xffff0000, v248
	v_lshlrev_b32_e32 v180, 16, v249
	v_and_b32_e32 v181, 0xffff0000, v249
	v_pk_fma_f32 v[22:23], v[22:23], v[126:127], v[172:173]
	v_pk_fma_f32 v[24:25], v[24:25], v[128:129], v[174:175]
	v_pk_fma_f32 v[14:15], v[14:15], v[118:119], v[178:179]
	v_pk_fma_f32 v[16:17], v[16:17], v[120:121], v[180:181]
	v_cvt_pk_bf16_f32 v22, v22, v23
	v_cvt_pk_bf16_f32 v23, v24, v25
	v_cvt_pk_bf16_f32 v24, v14, v15
	v_cvt_pk_bf16_f32 v25, v16, v17
	global_store_dwordx4 v[164:165], v[22:25], off offset:256
	s_waitcnt vmcnt(15)
	v_lshlrev_b32_e32 v172, 16, v182
	v_and_b32_e32 v173, 0xffff0000, v182
	v_lshlrev_b32_e32 v174, 16, v183
	v_and_b32_e32 v175, 0xffff0000, v183
	v_lshlrev_b32_e32 v178, 16, v184
	v_and_b32_e32 v179, 0xffff0000, v184
	v_lshlrev_b32_e32 v180, 16, v185
	v_and_b32_e32 v181, 0xffff0000, v185
	v_pk_fma_f32 v[18:19], v[18:19], v[134:135], v[172:173]
	v_pk_fma_f32 v[20:21], v[20:21], v[136:137], v[174:175]
	v_pk_fma_f32 v[10:11], v[10:11], v[130:131], v[178:179]
	v_pk_fma_f32 v[12:13], v[12:13], v[132:133], v[180:181]
	v_cvt_pk_bf16_f32 v18, v18, v19
	v_cvt_pk_bf16_f32 v19, v20, v21
	v_cvt_pk_bf16_f32 v20, v10, v11
	v_cvt_pk_bf16_f32 v21, v12, v13
	v_lshl_add_u64 v[164:165], v[164:165], 0, s[100:101]
	global_store_dwordx4 v[164:165], v[18:21], off
	s_waitcnt vmcnt(14)
	v_lshlrev_b32_e32 v172, 16, v186
	v_and_b32_e32 v173, 0xffff0000, v186
	v_lshlrev_b32_e32 v174, 16, v187
	v_and_b32_e32 v175, 0xffff0000, v187
	v_lshlrev_b32_e32 v178, 16, v188
	v_and_b32_e32 v179, 0xffff0000, v188
	v_lshlrev_b32_e32 v180, 16, v189
	v_and_b32_e32 v181, 0xffff0000, v189
	v_pk_fma_f32 v[6:7], v[6:7], v[126:127], v[172:173]
	v_pk_fma_f32 v[8:9], v[8:9], v[128:129], v[174:175]
	v_pk_fma_f32 v[2:3], v[2:3], v[118:119], v[178:179]
	v_pk_fma_f32 v[4:5], v[4:5], v[120:121], v[180:181]
	v_cvt_pk_bf16_f32 v6, v6, v7
	v_cvt_pk_bf16_f32 v7, v8, v9
	v_cvt_pk_bf16_f32 v8, v2, v3
	v_cvt_pk_bf16_f32 v9, v4, v5
	global_store_dwordx4 v[164:165], v[6:9], off offset:256
	s_cbranch_vccnz .LBB0_1623
	s_andn2_b64 vcc, exec, s[6:7]
	s_cbranch_vccnz .LBB0_1622
	s_barrier
	s_branch .LBB0_1622
